# s19
# speedup vs baseline: 1.0026x; 1.0026x over previous
.LBB1_12:
	s_waitcnt lgkmcnt(8)
	v_pk_add_f32 v[52:53], v[160:161], v[52:53]
	v_pk_add_f32 v[166:167], v[158:159], v[50:51]
	v_cvt_pk_f16_f32 v51, v52, v53
	s_waitcnt lgkmcnt(7)
	v_pk_add_f32 v[52:53], v[156:157], v[144:145]
	v_pk_add_f32 v[142:143], v[154:155], v[142:143]
	v_pk_add_f32 v[56:57], v[160:161], v[56:57]
	v_cvt_pk_f16_f32 v53, v52, v53
	v_cvt_pk_f16_f32 v52, v142, v143
	v_pk_add_f32 v[142:143], v[158:159], v[54:55]
	v_cvt_pk_f16_f32 v55, v56, v57
	v_pk_add_f32 v[56:57], v[156:157], v[140:141]
	v_pk_add_f32 v[138:139], v[154:155], v[138:139]
	v_pk_add_f32 v[60:61], v[160:161], v[60:61]
	v_cvt_pk_f16_f32 v57, v56, v57
	v_cvt_pk_f16_f32 v56, v138, v139
	v_pk_add_f32 v[138:139], v[158:159], v[58:59]
	v_cvt_pk_f16_f32 v59, v60, v61
	v_pk_add_f32 v[60:61], v[156:157], v[136:137]
	v_pk_add_f32 v[134:135], v[154:155], v[134:135]
	v_pk_add_f32 v[64:65], v[160:161], v[64:65]
	v_cvt_pk_f16_f32 v61, v60, v61
	v_cvt_pk_f16_f32 v60, v134, v135
	v_pk_add_f32 v[134:135], v[158:159], v[62:63]
	v_cvt_pk_f16_f32 v63, v64, v65
	v_pk_add_f32 v[64:65], v[156:157], v[128:129]
	v_pk_add_f32 v[126:127], v[154:155], v[126:127]
	s_waitcnt lgkmcnt(6)
	v_pk_add_f32 v[36:37], v[152:153], v[36:37]
	v_cvt_pk_f16_f32 v65, v64, v65
	v_cvt_pk_f16_f32 v64, v126, v127
	v_pk_add_f32 v[126:127], v[150:151], v[34:35]
	v_cvt_pk_f16_f32 v35, v36, v37
	s_waitcnt lgkmcnt(5)
	v_pk_add_f32 v[36:37], v[148:149], v[124:125]
	v_pk_add_f32 v[122:123], v[146:147], v[122:123]
	v_pk_add_f32 v[40:41], v[152:153], v[40:41]
	v_cvt_pk_f16_f32 v37, v36, v37
	v_cvt_pk_f16_f32 v36, v122, v123
	v_pk_add_f32 v[122:123], v[150:151], v[38:39]
	v_cvt_pk_f16_f32 v39, v40, v41
	v_pk_add_f32 v[40:41], v[148:149], v[120:121]
	v_pk_add_f32 v[118:119], v[146:147], v[118:119]
	v_pk_add_f32 v[44:45], v[152:153], v[44:45]
	v_cvt_pk_f16_f32 v41, v40, v41
	v_cvt_pk_f16_f32 v40, v118, v119
	v_pk_add_f32 v[118:119], v[150:151], v[42:43]
	v_cvt_pk_f16_f32 v43, v44, v45
	v_pk_add_f32 v[44:45], v[148:149], v[116:117]
	v_pk_add_f32 v[114:115], v[146:147], v[114:115]
	v_pk_add_f32 v[48:49], v[152:153], v[48:49]
	v_cvt_pk_f16_f32 v45, v44, v45
	v_cvt_pk_f16_f32 v44, v114, v115
	v_pk_add_f32 v[114:115], v[150:151], v[46:47]
	v_cvt_pk_f16_f32 v47, v48, v49
	v_pk_add_f32 v[48:49], v[148:149], v[112:113]
	v_pk_add_f32 v[110:111], v[146:147], v[110:111]
	s_waitcnt lgkmcnt(4)
	v_pk_add_f32 v[4:5], v[132:133], v[4:5]
	v_cvt_pk_f16_f32 v49, v48, v49
	v_cvt_pk_f16_f32 v48, v110, v111
	v_pk_add_f32 v[110:111], v[130:131], v[2:3]
	v_cvt_pk_f16_f32 v3, v4, v5
	s_waitcnt lgkmcnt(3)
	v_pk_add_f32 v[4:5], v[96:97], v[108:109]
	v_pk_add_f32 v[106:107], v[94:95], v[106:107]
	v_pk_add_f32 v[8:9], v[132:133], v[8:9]
	v_cvt_pk_f16_f32 v5, v4, v5
	v_cvt_pk_f16_f32 v4, v106, v107
	v_pk_add_f32 v[106:107], v[130:131], v[6:7]
	v_cvt_pk_f16_f32 v7, v8, v9
	v_pk_add_f32 v[8:9], v[96:97], v[104:105]
	v_pk_add_f32 v[102:103], v[94:95], v[102:103]
	v_cvt_pk_f16_f32 v9, v8, v9
	v_cvt_pk_f16_f32 v8, v102, v103
	v_pk_add_f32 v[102:103], v[130:131], v[14:15]
	v_lshrrev_b32_e32 v165, 4, v204
	v_cvt_pk_f16_f32 v14, v102, v103
	v_pk_add_f32 v[102:103], v[130:131], v[30:31]
	v_mul_i32_i24_e32 v30, 0xfff8, v208
	v_lshlrev_b32_e32 v31, 8, v174
	v_pk_add_f32 v[16:17], v[132:133], v[16:17]
	v_add3_u32 v124, v164, v30, v31
	v_xor_b32_e32 v30, v165, v174
	v_cvt_pk_f16_f32 v15, v16, v17
	v_pk_add_f32 v[16:17], v[96:97], v[100:101]
	v_pk_add_f32 v[98:99], v[94:95], v[98:99]
	v_lshl_add_u32 v177, v30, 4, v124
	v_cvt_pk_f16_f32 v17, v16, v17
	v_cvt_pk_f16_f32 v16, v98, v99
	ds_read_b128 v[98:101], v177
	v_cvt_pk_f16_f32 v38, v122, v123
	s_waitcnt lgkmcnt(3)
	v_pk_add_f32 v[122:123], v[90:91], v[10:11]
	v_bitop3_b32 v10, v165, v174, 4 bitop3:0x36
	v_pk_add_f32 v[32:33], v[132:133], v[32:33]
	v_lshl_add_u32 v194, v10, 4, v124
	v_cvt_pk_f16_f32 v46, v114, v115
	v_cvt_pk_f16_f32 v2, v110, v111
	v_cvt_pk_f16_f32 v6, v106, v107
	v_cvt_pk_f16_f32 v31, v32, v33
	v_cvt_pk_f16_f32 v30, v102, v103
	v_pk_add_f32 v[32:33], v[96:97], v[88:89]
	ds_read_b128 v[102:105], v176 offset:32768
	v_pk_add_f32 v[110:111], v[94:95], v[86:87]
	ds_read_b128 v[94:97], v176 offset:32832
	ds_read_b128 v[106:109], v177 offset:4096
	ds_read_b128 v[114:117], v194
	v_cvt_pk_f16_f32 v54, v142, v143
	v_cvt_pk_f16_f32 v33, v32, v33
	v_cvt_pk_f16_f32 v32, v110, v111
	s_waitcnt lgkmcnt(3)
	v_mfma_f32_16x16x32_f16 v[110:113], v[98:101], v[54:57], v[102:105]
	v_cvt_pk_f16_f32 v50, v166, v167
	v_cvt_pk_f16_f32 v58, v138, v139
	v_cvt_pk_f16_f32 v62, v134, v135
	v_pk_add_f32 v[12:13], v[92:93], v[12:13]
	v_cvt_pk_f16_f32 v10, v122, v123
	v_pk_add_f32 v[122:123], v[90:91], v[18:19]
	v_bitop3_b32 v18, v165, v174, 8 bitop3:0x36
	v_cvt_pk_f16_f32 v42, v118, v119
	v_mfma_f32_16x16x32_f16 v[86:89], v[98:101], v[50:53], v[102:105]
	v_cvt_pk_f16_f32 v11, v12, v13
	v_pk_add_f32 v[12:13], v[84:85], v[80:81]
	v_lshl_add_u32 v198, v18, 4, v124
	v_mfma_f32_16x16x32_f16 v[118:121], v[98:101], v[58:61], v[102:105]
	v_cvt_pk_f16_f32 v13, v12, v13
	v_cvt_pk_f16_f32 v34, v126, v127
	v_pk_add_f32 v[126:127], v[90:91], v[22:23]
	v_mfma_f32_16x16x32_f16 v[98:101], v[98:101], v[62:65], v[102:105]
	v_bitop3_b32 v22, v165, v174, 12 bitop3:0x36
	v_lshl_add_u32 v199, v22, 4, v124
	v_cvt_pk_f16_f32 v18, v122, v123
	v_pk_add_f32 v[102:103], v[82:83], v[78:79]
	ds_read_b128 v[78:81], v194 offset:4096
	v_cvt_pk_f16_f32 v12, v102, v103
	s_waitcnt lgkmcnt(1)
	v_mfma_f32_16x16x32_f16 v[102:105], v[114:117], v[38:41], v[110:113]
	ds_read_b128 v[122:125], v199
	v_pk_add_f32 v[20:21], v[92:93], v[20:21]
	v_pk_add_f32 v[28:29], v[92:93], v[28:29]
	ds_read_b128 v[110:113], v198
	v_mfma_f32_16x16x32_f16 v[98:101], v[114:117], v[46:49], v[98:101]
	v_cvt_pk_f16_f32 v19, v20, v21
	v_pk_add_f32 v[20:21], v[84:85], v[76:77]
	v_pk_add_f32 v[90:91], v[90:91], v[26:27]
	v_mfma_f32_16x16x32_f16 v[86:89], v[114:117], v[34:37], v[86:89]
	v_cvt_pk_f16_f32 v27, v28, v29
	v_pk_add_f32 v[28:29], v[84:85], v[68:69]
	v_pk_add_f32 v[66:67], v[82:83], v[66:67]
	v_mfma_f32_16x16x32_f16 v[118:121], v[114:117], v[42:45], v[118:121]
	v_add_f32_e64 v114, v82, v74
	v_add_f32_e64 v115, v83, v75
	ds_read_b128 v[74:77], v198 offset:4096
	v_pk_add_f32 v[24:25], v[92:93], v[24:25]
	s_waitcnt lgkmcnt(1)
	v_mfma_f32_16x16x32_f16 v[98:101], v[110:113], v[30:33], v[98:101]
	v_cvt_pk_f16_f32 v26, v90, v91
	v_cvt_pk_f16_f32 v29, v28, v29
	v_cvt_pk_f16_f32 v28, v66, v67
	v_cvt_pk_f16_f32 v21, v20, v21
	v_mfma_f32_16x16x32_f16 v[86:89], v[110:113], v[2:5], v[86:89]
	v_cvt_pk_f16_f32 v20, v114, v115
	v_cvt_pk_f16_f32 v23, v24, v25
	v_pk_add_f32 v[24:25], v[84:85], v[72:73]
	v_mfma_f32_16x16x32_f16 v[102:105], v[110:113], v[6:9], v[102:105]
	v_cvt_pk_f16_f32 v22, v126, v127
	v_cvt_pk_f16_f32 v25, v24, v25
	v_add_f32_e32 v212, v162, v163
	v_mfma_f32_16x16x32_f16 v[114:117], v[110:113], v[14:17], v[118:121]
	v_add_f32_e64 v110, v82, v70
	v_add_f32_e64 v111, v83, v71
	ds_read_b128 v[70:73], v199 offset:4096
	v_cvt_pk_f16_f32 v24, v110, v111
	v_mfma_f32_16x16x32_f16 v[66:69], v[122:125], v[26:29], v[98:101]
	v_add_u32_e32 v142, s77, v208
	v_ashrrev_i32_e32 v143, 31, v142
	v_lshlrev_b64 v[142:143], 13, v[142:143]
	v_mfma_f32_16x16x32_f16 v[82:85], v[106:109], v[50:53], v[94:97]
	s_waitcnt vmcnt(3)
	v_cmp_eq_u32_e64 s[0:1], 0, v213
	v_cmp_gt_u32_e32 vcc, 16, v204
	v_mfma_f32_16x16x32_f16 v[90:93], v[106:109], v[54:57], v[94:97]
	v_mfma_f32_16x16x32_f16 v[98:101], v[106:109], v[58:61], v[94:97]
	v_mfma_f32_16x16x32_f16 v[94:97], v[106:109], v[62:65], v[94:97]
	v_mfma_f32_16x16x32_f16 v[82:85], v[78:81], v[34:37], v[82:85]
	v_mfma_f32_16x16x32_f16 v[90:93], v[78:81], v[38:41], v[90:93]
	v_mfma_f32_16x16x32_f16 v[98:101], v[78:81], v[42:45], v[98:101]
	v_mfma_f32_16x16x32_f16 v[78:81], v[78:81], v[46:49], v[94:97]
	s_waitcnt lgkmcnt(1)
	v_mfma_f32_16x16x32_f16 v[82:85], v[74:77], v[2:5], v[82:85]
	v_mfma_f32_16x16x32_f16 v[90:93], v[74:77], v[6:9], v[90:93]
	v_mfma_f32_16x16x32_f16 v[98:101], v[74:77], v[14:17], v[98:101]
	v_mfma_f32_16x16x32_f16 v[74:77], v[74:77], v[30:33], v[78:81]
	s_nop 2
	ds_read_b128 v[78:81], v177 offset:8192
	s_waitcnt lgkmcnt(1)
	v_mfma_f32_16x16x32_f16 v[94:97], v[70:73], v[10:13], v[82:85]
	v_mfma_f32_16x16x32_f16 v[154:157], v[70:73], v[18:21], v[90:93]
	v_mfma_f32_16x16x32_f16 v[106:109], v[70:73], v[22:25], v[98:101]
	s_nop 5
	v_exp_f32_e32 v94, v94
	v_exp_f32_e32 v95, v95
	v_add_f32_e32 v94, 1.0, v94
	v_mfma_f32_16x16x32_f16 v[70:73], v[70:73], v[26:29], v[74:77]
	s_nop 2
	ds_read_b128 v[74:77], v176 offset:32896
	ds_read_b128 v[82:85], v176 offset:32960
	ds_read_b128 v[90:93], v177 offset:12288
	v_rcp_f32_e32 v94, v94
	v_add_f32_e32 v95, 1.0, v95
	v_mfma_f32_16x16x32_f16 v[158:161], v[122:125], v[18:21], v[102:105]
	v_rcp_f32_e32 v95, v95
	s_waitcnt lgkmcnt(2)
	v_mfma_f32_16x16x32_f16 v[98:101], v[78:81], v[50:53], v[74:77]
	v_mfma_f32_16x16x32_f16 v[102:105], v[78:81], v[54:57], v[74:77]
	v_mfma_f32_16x16x32_f16 v[110:113], v[78:81], v[58:61], v[74:77]
	v_mfma_f32_16x16x32_f16 v[74:77], v[78:81], v[62:65], v[74:77]
	ds_read_b128 v[78:81], v194 offset:8192
	ds_read_b128 v[118:121], v194 offset:12288
	v_mfma_f32_16x16x32_f16 v[86:89], v[122:125], v[10:13], v[86:89]
	v_mfma_f32_16x16x32_f16 v[114:117], v[122:125], v[22:25], v[114:117]
	s_waitcnt lgkmcnt(1)
	v_mfma_f32_16x16x32_f16 v[98:101], v[78:81], v[34:37], v[98:101]
	s_nop 4
	v_exp_f32_e32 v86, v86
	v_exp_f32_e32 v87, v87
	v_add_f32_e32 v86, 1.0, v86
	v_mfma_f32_16x16x32_f16 v[102:105], v[78:81], v[38:41], v[102:105]
	v_rcp_f32_e32 v86, v86
	v_add_f32_e32 v87, 1.0, v87
	v_rcp_f32_e32 v87, v87
	v_mfma_f32_16x16x32_f16 v[110:113], v[78:81], v[42:45], v[110:113]
	v_mfma_f32_16x16x32_f16 v[74:77], v[78:81], v[46:49], v[74:77]
	ds_read_b128 v[78:81], v198 offset:8192
	ds_read_b128 v[122:125], v198 offset:12288
	s_waitcnt lgkmcnt(1)
	v_mfma_f32_16x16x32_f16 v[98:101], v[78:81], v[2:5], v[98:101]
	v_mfma_f32_16x16x32_f16 v[102:105], v[78:81], v[6:9], v[102:105]
	v_mfma_f32_16x16x32_f16 v[110:113], v[78:81], v[14:17], v[110:113]
	v_mfma_f32_16x16x32_f16 v[74:77], v[78:81], v[30:33], v[74:77]
	ds_read_b128 v[78:81], v199 offset:8192
	ds_read_b128 v[126:129], v199 offset:12288
	s_waitcnt lgkmcnt(1)
	v_mfma_f32_16x16x32_f16 v[130:133], v[78:81], v[10:13], v[98:101]
	v_mfma_f32_16x16x32_f16 v[98:101], v[90:93], v[54:57], v[82:85]
	s_nop 6
	v_exp_f32_e32 v131, v131
	s_nop 0
	v_add_f32_e32 v131, 1.0, v131
	v_mfma_f32_16x16x32_f16 v[170:173], v[78:81], v[18:21], v[102:105]
	v_rcp_f32_e32 v131, v131
	v_mfma_f32_16x16x32_f16 v[138:141], v[78:81], v[22:25], v[110:113]
	v_mfma_f32_16x16x32_f16 v[74:77], v[78:81], v[26:29], v[74:77]
	v_mfma_f32_16x16x32_f16 v[78:81], v[90:93], v[50:53], v[82:85]
	v_mfma_f32_16x16x32_f16 v[102:105], v[90:93], v[58:61], v[82:85]
	v_mfma_f32_16x16x32_f16 v[82:85], v[90:93], v[62:65], v[82:85]
	v_mfma_f32_16x16x32_f16 v[90:93], v[118:121], v[38:41], v[98:101]
	v_mfma_f32_16x16x32_f16 v[90:93], v[122:125], v[6:9], v[90:93]
	v_mfma_f32_16x16x32_f16 v[78:81], v[118:121], v[34:37], v[78:81]
	v_mfma_f32_16x16x32_f16 v[98:101], v[118:121], v[42:45], v[102:105]
	v_mfma_f32_16x16x32_f16 v[82:85], v[118:121], v[46:49], v[82:85]
	s_waitcnt lgkmcnt(0)
	v_mfma_f32_16x16x32_f16 v[166:169], v[126:129], v[18:21], v[90:93]
	s_nop 2
	ds_read_b128 v[90:93], v177 offset:16384
	v_mfma_f32_16x16x32_f16 v[78:81], v[122:125], v[2:5], v[78:81]
	v_mfma_f32_16x16x32_f16 v[98:101], v[122:125], v[14:17], v[98:101]
	v_mfma_f32_16x16x32_f16 v[82:85], v[122:125], v[30:33], v[82:85]
	v_mfma_f32_16x16x32_f16 v[110:113], v[126:129], v[10:13], v[78:81]
	v_mfma_f32_16x16x32_f16 v[134:137], v[126:129], v[22:25], v[98:101]
	v_mfma_f32_16x16x32_f16 v[78:81], v[126:129], v[26:29], v[82:85]
	s_nop 4
	ds_read_b128 v[82:85], v176 offset:33024
	ds_read_b128 v[98:101], v176 offset:33088
	ds_read_b128 v[118:121], v177 offset:20480
	v_exp_f32_e32 v110, v110
	v_exp_f32_e32 v111, v111
	s_waitcnt lgkmcnt(2)
	v_mfma_f32_16x16x32_f16 v[102:105], v[90:93], v[50:53], v[82:85]
	v_add_f32_e32 v110, 1.0, v110
	v_rcp_f32_e32 v110, v110
	v_mfma_f32_16x16x32_f16 v[122:125], v[90:93], v[54:57], v[82:85]
	v_add_f32_e32 v111, 1.0, v111
	v_mfma_f32_16x16x32_f16 v[126:129], v[90:93], v[58:61], v[82:85]
	v_mfma_f32_16x16x32_f16 v[82:85], v[90:93], v[62:65], v[82:85]
	ds_read_b128 v[90:93], v194 offset:16384
	ds_read_b128 v[150:153], v194 offset:20480
	ds_read_b128 v[162:165], v198 offset:20480
	ds_read_b128 v[182:185], v199 offset:16384
	s_waitcnt lgkmcnt(3)
	v_mfma_f32_16x16x32_f16 v[102:105], v[90:93], v[34:37], v[102:105]
	v_mfma_f32_16x16x32_f16 v[122:125], v[90:93], v[38:41], v[122:125]
	v_mfma_f32_16x16x32_f16 v[126:129], v[90:93], v[42:45], v[126:129]
	v_mfma_f32_16x16x32_f16 v[82:85], v[90:93], v[46:49], v[82:85]
	ds_read_b128 v[90:93], v198 offset:16384
	s_waitcnt lgkmcnt(0)
	v_mfma_f32_16x16x32_f16 v[144:147], v[90:93], v[2:5], v[102:105]
	s_nop 2
	ds_read_b128 v[102:105], v176 offset:33792
	s_waitcnt lgkmcnt(0)
	v_fma_f32 v242, v102, v86, 0
	v_exp_f32_e32 v86, v88
	v_fmac_f32_e32 v242, v103, v87
	v_exp_f32_e32 v87, v89
	v_mfma_f32_16x16x32_f16 v[122:125], v[90:93], v[6:9], v[122:125]
	v_add_f32_e32 v86, 1.0, v86
	v_rcp_f32_e32 v86, v86
	v_add_f32_e32 v87, 1.0, v87
	v_rcp_f32_e32 v87, v87
	v_mfma_f32_16x16x32_f16 v[126:129], v[90:93], v[14:17], v[126:129]
	v_fmac_f32_e32 v242, v104, v86
	v_fmac_f32_e32 v242, v105, v87
	v_mfma_f32_16x16x32_f16 v[82:85], v[90:93], v[30:33], v[82:85]
	ds_read_b128 v[90:93], v176 offset:33856
	ds_read_b128 v[186:189], v199 offset:20480
	s_waitcnt lgkmcnt(1)
	v_fmac_f32_e32 v242, v90, v94
	v_exp_f32_e32 v94, v96
	v_mfma_f32_16x16x32_f16 v[190:193], v[182:185], v[10:13], v[144:147]
	v_fmac_f32_e32 v242, v91, v95
	s_nop 1
	v_exp_f32_e32 v144, v97
	v_mfma_f32_16x16x32_f16 v[86:89], v[118:121], v[50:53], v[98:101]
	v_add_f32_e32 v145, 1.0, v94
	v_mfma_f32_16x16x32_f16 v[178:181], v[182:185], v[18:21], v[122:125]
	v_mfma_f32_16x16x32_f16 v[146:149], v[182:185], v[22:25], v[126:129]
	v_mfma_f32_16x16x32_f16 v[122:125], v[118:121], v[54:57], v[98:101]
	v_mfma_f32_16x16x32_f16 v[126:129], v[118:121], v[58:61], v[98:101]
	v_mfma_f32_16x16x32_f16 v[94:97], v[118:121], v[62:65], v[98:101]
	s_nop 2
	v_rcp_f32_e32 v98, v145
	v_add_f32_e32 v99, 1.0, v144
	v_rcp_f32_e32 v99, v99
	v_mfma_f32_16x16x32_f16 v[118:121], v[150:153], v[34:37], v[86:89]
	v_fmac_f32_e32 v242, v92, v98
	v_exp_f32_e32 v144, v190
	v_fmac_f32_e32 v242, v93, v99
	v_exp_f32_e32 v86, v130
	ds_read_b128 v[98:101], v176 offset:33920
	v_mfma_f32_16x16x32_f16 v[122:125], v[150:153], v[38:41], v[122:125]
	v_add_f32_e32 v144, 1.0, v144
	v_add_f32_e32 v86, 1.0, v86
	v_rcp_f32_e32 v130, v86
	ds_read_b128 v[86:89], v176 offset:33984
	v_mfma_f32_16x16x32_f16 v[118:121], v[162:165], v[2:5], v[118:121]
	v_rcp_f32_e32 v144, v144
	s_waitcnt lgkmcnt(1)
	v_fmac_f32_e32 v242, v98, v130
	v_exp_f32_e32 v130, v132
	v_fmac_f32_e32 v242, v99, v131
	v_exp_f32_e32 v131, v133
	v_mfma_f32_16x16x32_f16 v[122:125], v[162:165], v[6:9], v[122:125]
	v_add_f32_e32 v130, 1.0, v130
	v_rcp_f32_e32 v130, v130
	v_mfma_f32_16x16x32_f16 v[126:129], v[150:153], v[42:45], v[126:129]
	v_fmac_f32_e32 v242, v100, v130
	v_add_f32_e32 v130, 1.0, v131
	v_rcp_f32_e32 v130, v130
	v_mfma_f32_16x16x32_f16 v[94:97], v[150:153], v[46:49], v[94:97]
	v_fmac_f32_e32 v242, v101, v130
	s_waitcnt lgkmcnt(0)
	v_fmac_f32_e32 v242, v86, v110
	v_exp_f32_e32 v110, v112
	v_mfma_f32_16x16x32_f16 v[130:133], v[186:189], v[10:13], v[118:121]
	v_add_f32_e32 v110, 1.0, v110
	s_nop 1
	v_exp_f32_e32 v119, v113
	v_mfma_f32_16x16x32_f16 v[82:85], v[182:185], v[26:29], v[82:85]
	v_rcp_f32_e32 v118, v111
	v_rcp_f32_e32 v120, v110
	v_add_f32_e32 v119, 1.0, v119
	v_mfma_f32_16x16x32_f16 v[182:185], v[186:189], v[18:21], v[122:125]
	v_rcp_f32_e32 v119, v119
	ds_read_b128 v[110:113], v176 offset:33152
	v_fmac_f32_e32 v242, v87, v118
	ds_read_b128 v[122:125], v177 offset:24576
	v_mfma_f32_16x16x32_f16 v[126:129], v[162:165], v[14:17], v[126:129]
	v_fmac_f32_e32 v242, v88, v120
	ds_read_b128 v[214:217], v176 offset:33216
	ds_read_b128 v[218:221], v177 offset:28672
	v_fmac_f32_e32 v242, v89, v119
	v_mfma_f32_16x16x32_f16 v[94:97], v[162:165], v[30:33], v[94:97]
	ds_read_b128 v[118:121], v176 offset:34048
	v_exp_f32_e32 v130, v130
	ds_read_b128 v[226:229], v194 offset:28672
	v_mfma_f32_16x16x32_f16 v[150:153], v[186:189], v[22:25], v[126:129]
	v_exp_f32_e32 v131, v131
	s_waitcnt lgkmcnt(1)
	v_fmac_f32_e32 v242, v118, v144
	v_exp_f32_e32 v144, v193
	v_mfma_f32_16x16x32_f16 v[94:97], v[186:189], v[26:29], v[94:97]
	ds_read_b128 v[186:189], v194 offset:24576
	v_add_f32_e32 v130, 1.0, v130
	v_add_f32_e32 v144, 1.0, v144
	v_mfma_f32_16x16x32_f16 v[126:129], v[122:125], v[50:53], v[110:113]
	v_rcp_f32_e32 v144, v144
	v_rcp_f32_e32 v130, v130
	v_lshlrev_b32_e32 v194, 2, v175
	v_mfma_f32_16x16x32_f16 v[162:165], v[122:125], v[54:57], v[110:113]
	v_mfma_f32_16x16x32_f16 v[222:225], v[122:125], v[58:61], v[110:113]
	v_mfma_f32_16x16x32_f16 v[122:125], v[122:125], v[62:65], v[110:113]
	s_nop 2
	v_exp_f32_e32 v110, v191
	v_exp_f32_e32 v111, v192
	s_waitcnt lgkmcnt(0)
	v_mfma_f32_16x16x32_f16 v[126:129], v[186:189], v[34:37], v[126:129]
	v_add_f32_e32 v110, 1.0, v110
	v_rcp_f32_e32 v145, v110
	v_add_f32_e32 v110, 1.0, v111
	v_rcp_f32_e32 v177, v110
	ds_read_b128 v[110:113], v176 offset:34112
	ds_read_b128 v[230:233], v198 offset:24576
	ds_read_b128 v[190:193], v198 offset:28672
	ds_read_b128 v[234:237], v199 offset:24576
	v_fmac_f32_e32 v242, v119, v145
	v_mfma_f32_16x16x32_f16 v[122:125], v[186:189], v[46:49], v[122:125]
	v_fmac_f32_e32 v242, v120, v177
	v_fmac_f32_e32 v242, v121, v144
	s_waitcnt lgkmcnt(3)
	v_fmac_f32_e32 v242, v110, v130
	s_waitcnt lgkmcnt(2)
	v_mfma_f32_16x16x32_f16 v[126:129], v[230:233], v[2:5], v[126:129]
	v_add_f32_e32 v130, 1.0, v131
	v_rcp_f32_e32 v130, v130
	v_exp_f32_e32 v131, v132
	v_mfma_f32_16x16x32_f16 v[162:165], v[186:189], v[38:41], v[162:165]
	v_fmac_f32_e32 v242, v111, v130
	v_mfma_f32_16x16x32_f16 v[222:225], v[186:189], v[42:45], v[222:225]
	v_mfma_f32_16x16x32_f16 v[122:125], v[230:233], v[30:33], v[122:125]
	s_waitcnt lgkmcnt(0)
	v_mfma_f32_16x16x32_f16 v[238:241], v[234:237], v[10:13], v[126:129]
	s_nop 2
	v_exp_f32_e32 v126, v133
	v_mfma_f32_16x16x32_f16 v[162:165], v[230:233], v[6:9], v[162:165]
	v_add_f32_e32 v127, 1.0, v131
	v_rcp_f32_e32 v127, v127
	v_add_f32_e32 v126, 1.0, v126
	v_mfma_f32_16x16x32_f16 v[222:225], v[230:233], v[14:17], v[222:225]
	v_rcp_f32_e32 v126, v126
	v_exp_f32_e32 v144, v238
	ds_read_b128 v[230:233], v199 offset:28672
	v_mfma_f32_16x16x32_f16 v[130:133], v[234:237], v[26:29], v[122:125]
	v_fmac_f32_e32 v242, v112, v127
	v_fmac_f32_e32 v242, v113, v126
	ds_read_b128 v[126:129], v176 offset:34176
	v_mfma_f32_16x16x32_f16 v[122:125], v[218:221], v[50:53], v[214:217]
	v_exp_f32_e32 v145, v239
	v_add_f32_e32 v144, 1.0, v144
	v_rcp_f32_e32 v144, v144
	v_mfma_f32_16x16x32_f16 v[186:189], v[234:237], v[18:21], v[162:165]
	v_exp_f32_e32 v177, v240
	v_add_f32_e32 v145, 1.0, v145
	v_rcp_f32_e32 v145, v145
	v_mfma_f32_16x16x32_f16 v[162:165], v[234:237], v[22:25], v[222:225]
	v_mfma_f32_16x16x32_f16 v[222:225], v[226:229], v[34:37], v[122:125]
	v_mfma_f32_16x16x32_f16 v[222:225], v[190:193], v[2:5], v[222:225]
	s_nop 1
	ds_read_b128 v[122:125], v176 offset:34240
	s_waitcnt lgkmcnt(1)
	v_fmac_f32_e32 v242, v126, v144
	v_add_f32_e32 v144, 1.0, v177
	v_rcp_f32_e32 v144, v144
	v_mfma_f32_16x16x32_f16 v[222:225], v[230:233], v[10:13], v[222:225]
	v_fmac_f32_e32 v242, v127, v145
	v_exp_f32_e32 v145, v241
	v_fmac_f32_e32 v242, v128, v144
	v_mfma_f32_16x16x32_f16 v[238:241], v[218:221], v[58:61], v[214:217]
	v_add_f32_e32 v145, 1.0, v145
	s_nop 2
	v_exp_f32_e32 v144, v222
	v_rcp_f32_e32 v145, v145
	v_exp_f32_e32 v176, v223
	v_mfma_f32_16x16x32_f16 v[234:237], v[218:221], v[54:57], v[214:217]
	v_add_f32_e32 v144, 1.0, v144
	v_rcp_f32_e32 v144, v144
	v_fmac_f32_e32 v242, v129, v145
	v_exp_f32_e32 v145, v224
	v_mfma_f32_16x16x32_f16 v[214:217], v[218:221], v[62:65], v[214:217]
	s_waitcnt lgkmcnt(0)
	v_fmac_f32_e32 v242, v122, v144
	v_add_f32_e32 v144, 1.0, v176
	v_exp_f32_e32 v176, v225
	v_rcp_f32_e32 v144, v144
	v_add_f32_e32 v145, 1.0, v145
	v_rcp_f32_e32 v145, v145
	v_add_f32_e32 v176, 1.0, v176
	v_rcp_f32_e32 v176, v176
	v_fmac_f32_e32 v242, v123, v144
	v_fmac_f32_e32 v242, v124, v145
	v_mfma_f32_16x16x32_f16 v[222:225], v[226:229], v[42:45], v[238:241]
	v_fmac_f32_e32 v242, v125, v176
	v_mov_b32_e32 v198, v242
	v_lshl_add_u64 v[176:177], s[18:19], 0, v[142:143]
	v_mfma_f32_16x16x32_f16 v[142:145], v[190:193], v[14:17], v[222:225]
	v_lshl_add_u64 v[176:177], v[176:177], 0, v[194:195]
	v_lshlrev_b32_e32 v194, 2, v174
	s_waitcnt lgkmcnt(0)
	s_nop 1
	v_permlane16_swap_b32_e32 v198, v242
	v_add_f32_e32 v175, v242, v198
	v_mov_b32_e32 v222, v175
	v_mfma_f32_16x16x32_f16 v[218:221], v[226:229], v[38:41], v[234:237]
	v_lshl_add_u64 v[198:199], v[176:177], 0, v[194:195]
	s_waitcnt lgkmcnt(0)
	s_nop 1
	v_permlane32_swap_b32_e32 v222, v175
	v_add_f32_e32 v174, v175, v222
	v_mfma_f32_16x16x32_f16 v[214:217], v[226:229], v[46:49], v[214:217]
	v_add_f32_e32 v174, v212, v174
	v_mul_f32_e32 v174, 0x3fb8aa3b, v174
	v_exp_f32_e32 v194, v174
	v_mfma_f32_16x16x32_f16 v[218:221], v[190:193], v[6:9], v[218:221]
	v_cndmask_b32_e64 v194, 0, v194, s[0:1]
	v_mfma_f32_16x16x32_f16 v[214:217], v[190:193], v[30:33], v[214:217]
	v_mfma_f32_16x16x32_f16 v[190:193], v[230:233], v[18:21], v[218:221]
	v_mfma_f32_16x16x32_f16 v[174:177], v[230:233], v[22:25], v[142:145]
	v_mfma_f32_16x16x32_f16 v[142:145], v[230:233], v[26:29], v[214:217]
	s_and_saveexec_b64 s[0:1], vcc
	s_cbranch_execz .LBB1_14
	global_store_dword v[198:199], v194, off
.LBB1_14:
	s_or_b64 exec, exec, s[0:1]
	s_cmp_lg_u32 s2, 0x1800000
	s_cselect_b32 s32, 0x800000, 0
	s_add_u32 s100, s22, s32
	s_addc_u32 s101, s90, 0
	global_load_dwordx4 v[216:219], v201, s[100:101] nt
	s_add_u32 s100, s22, s32
	s_addc_u32 s101, s90, 0
	s_add_u32 s100, s100, 0x20000
	s_addc_u32 s101, s101, 0
	global_load_dwordx4 v[220:223], v201, s[100:101] nt
	s_add_u32 s100, s22, s32
	s_addc_u32 s101, s90, 0
	s_add_u32 s100, s100, 0x40000
	s_addc_u32 s101, s101, 0
	global_load_dwordx4 v[224:227], v201, s[100:101] nt
	s_add_u32 s100, s22, s32
	s_addc_u32 s101, s90, 0
	s_add_u32 s100, s100, 0x60000
	s_addc_u32 s101, s101, 0
	global_load_dwordx4 v[228:231], v201, s[100:101] nt
	s_add_u32 s100, s22, s32
	s_addc_u32 s101, s90, 0
	s_add_u32 s100, s100, 0x80000
	s_addc_u32 s101, s101, 0
	global_load_dwordx4 v[232:235], v201, s[100:101] nt
	s_add_u32 s100, s22, s32
	s_addc_u32 s101, s90, 0
	s_add_u32 s100, s100, 0xa0000
	s_addc_u32 s101, s101, 0
	global_load_dwordx4 v[236:239], v201, s[100:101] nt
	s_add_u32 s100, s22, s32
	s_addc_u32 s101, s90, 0
	s_add_u32 s100, s100, 0xc0000
	s_addc_u32 s101, s101, 0
	global_load_dwordx4 v[240:243], v201, s[100:101] nt
	s_add_u32 s100, s22, s32
	s_addc_u32 s101, s90, 0
	s_add_u32 s100, s100, 0xe0000
	s_addc_u32 s101, s101, 0
	global_load_dwordx4 v[244:247], v201, s[100:101] nt
	v_exp_f32_e32 v154, v154
	v_exp_f32_e32 v155, v155
	v_exp_f32_e32 v156, v156
	v_exp_f32_e32 v157, v157
	v_pk_add_f32 v[154:155], v[154:155], 1.0 op_sel_hi:[1,0]
	v_pk_add_f32 v[156:157], v[156:157], 1.0 op_sel_hi:[1,0]
	v_rcp_f32_e32 v154, v154
	v_rcp_f32_e32 v155, v155
	v_rcp_f32_e32 v156, v156
	v_rcp_f32_e32 v157, v157
	v_pk_mul_f32 v[248:249], v[154:155], v[90:91]
	v_pk_fma_f32 v[248:249], v[156:157], v[92:93], v[248:249]
	v_exp_f32_e32 v158, v158
	v_exp_f32_e32 v159, v159
	v_exp_f32_e32 v160, v160
	v_exp_f32_e32 v161, v161
	v_pk_add_f32 v[158:159], v[158:159], 1.0 op_sel_hi:[1,0]
	v_pk_add_f32 v[160:161], v[160:161], 1.0 op_sel_hi:[1,0]
	v_rcp_f32_e32 v158, v158
	v_rcp_f32_e32 v159, v159
	v_rcp_f32_e32 v160, v160
	v_rcp_f32_e32 v161, v161
	v_pk_fma_f32 v[248:249], v[158:159], v[102:103], v[248:249]
	v_pk_fma_f32 v[248:249], v[160:161], v[104:105], v[248:249]
	v_exp_f32_e32 v166, v166
	v_exp_f32_e32 v167, v167
	v_exp_f32_e32 v168, v168
	v_exp_f32_e32 v169, v169
	v_pk_add_f32 v[166:167], v[166:167], 1.0 op_sel_hi:[1,0]
	v_pk_add_f32 v[168:169], v[168:169], 1.0 op_sel_hi:[1,0]
	v_rcp_f32_e32 v166, v166
	v_rcp_f32_e32 v167, v167
	v_rcp_f32_e32 v168, v168
	v_rcp_f32_e32 v169, v169
	v_pk_fma_f32 v[248:249], v[166:167], v[86:87], v[248:249]
	v_pk_fma_f32 v[248:249], v[168:169], v[88:89], v[248:249]
	v_exp_f32_e32 v170, v170
	v_exp_f32_e32 v171, v171
	v_exp_f32_e32 v172, v172
	v_exp_f32_e32 v173, v173
	v_pk_add_f32 v[170:171], v[170:171], 1.0 op_sel_hi:[1,0]
	v_pk_add_f32 v[172:173], v[172:173], 1.0 op_sel_hi:[1,0]
	v_rcp_f32_e32 v170, v170
	v_rcp_f32_e32 v171, v171
	v_rcp_f32_e32 v172, v172
	v_rcp_f32_e32 v173, v173
	v_pk_fma_f32 v[248:249], v[170:171], v[98:99], v[248:249]
	v_pk_fma_f32 v[248:249], v[172:173], v[100:101], v[248:249]
	v_exp_f32_e32 v178, v178
	v_exp_f32_e32 v179, v179
	v_exp_f32_e32 v180, v180
	v_exp_f32_e32 v181, v181
	v_pk_add_f32 v[178:179], v[178:179], 1.0 op_sel_hi:[1,0]
	v_pk_add_f32 v[180:181], v[180:181], 1.0 op_sel_hi:[1,0]
	v_rcp_f32_e32 v178, v178
	v_rcp_f32_e32 v179, v179
	v_rcp_f32_e32 v180, v180
	v_rcp_f32_e32 v181, v181
	v_pk_fma_f32 v[248:249], v[178:179], v[118:119], v[248:249]
	v_pk_fma_f32 v[248:249], v[180:181], v[120:121], v[248:249]
	v_exp_f32_e32 v182, v182
	v_exp_f32_e32 v183, v183
	v_exp_f32_e32 v184, v184
	v_exp_f32_e32 v185, v185
	v_pk_add_f32 v[182:183], v[182:183], 1.0 op_sel_hi:[1,0]
	v_pk_add_f32 v[184:185], v[184:185], 1.0 op_sel_hi:[1,0]
	v_rcp_f32_e32 v182, v182
	v_rcp_f32_e32 v183, v183
	v_rcp_f32_e32 v184, v184
	v_rcp_f32_e32 v185, v185
	v_pk_fma_f32 v[248:249], v[182:183], v[110:111], v[248:249]
	v_pk_fma_f32 v[248:249], v[184:185], v[112:113], v[248:249]
	v_exp_f32_e32 v186, v186
	v_exp_f32_e32 v187, v187
	v_exp_f32_e32 v188, v188
	v_exp_f32_e32 v189, v189
	v_pk_add_f32 v[186:187], v[186:187], 1.0 op_sel_hi:[1,0]
	v_pk_add_f32 v[188:189], v[188:189], 1.0 op_sel_hi:[1,0]
	v_rcp_f32_e32 v186, v186
	v_rcp_f32_e32 v187, v187
	v_rcp_f32_e32 v188, v188
	v_rcp_f32_e32 v189, v189
	v_pk_fma_f32 v[248:249], v[186:187], v[126:127], v[248:249]
	v_pk_fma_f32 v[248:249], v[188:189], v[128:129], v[248:249]
	v_exp_f32_e32 v190, v190
	v_exp_f32_e32 v191, v191
	v_exp_f32_e32 v192, v192
	v_exp_f32_e32 v193, v193
	v_pk_add_f32 v[190:191], v[190:191], 1.0 op_sel_hi:[1,0]
	v_pk_add_f32 v[192:193], v[192:193], 1.0 op_sel_hi:[1,0]
	v_rcp_f32_e32 v190, v190
	v_rcp_f32_e32 v191, v191
	v_rcp_f32_e32 v192, v192
	v_rcp_f32_e32 v193, v193
	v_pk_fma_f32 v[248:249], v[190:191], v[122:123], v[248:249]
	v_pk_fma_f32 v[248:249], v[192:193], v[124:125], v[248:249]
	v_add_f32_e32 v158, v248, v249
	v_mov_b32_e32 v154, v158
	s_waitcnt vmcnt(10)
	v_cmp_eq_u32_e64 s[0:1], 0, v211
	s_waitcnt lgkmcnt(0)
	s_nop 1
	v_permlane16_swap_b32_e32 v154, v158
	v_add_f32_e32 v154, v158, v154
	v_mov_b32_e32 v155, v154
	s_waitcnt lgkmcnt(0)
	s_nop 1
	v_permlane32_swap_b32_e32 v155, v154
	v_add_f32_e32 v154, v154, v155
	v_add_f32_e32 v154, v212, v154
	v_mul_f32_e32 v154, 0x3fb8aa3b, v154
	v_exp_f32_e32 v154, v154
	s_nop 0
	v_cndmask_b32_e64 v154, 0, v154, s[0:1]
	s_and_saveexec_b64 s[0:1], vcc
	s_cbranch_execz .LBB1_16
	global_store_dword v[198:199], v154, off offset:64
.LBB1_16:
	s_or_b64 exec, exec, s[0:1]
	s_add_u32 s100, s22, s32
	s_addc_u32 s101, s90, 0
	s_add_u32 s100, s100, 0x100
	s_addc_u32 s101, s101, 0
	global_load_dwordx4 v[156:159], v201, s[100:101] nt
	s_add_u32 s100, s22, s32
	s_addc_u32 s101, s90, 0
	s_add_u32 s100, s100, 0x20100
	s_addc_u32 s101, s101, 0
	global_load_dwordx4 v[168:171], v201, s[100:101] nt
	s_add_u32 s100, s22, s32
	s_addc_u32 s101, s90, 0
	s_add_u32 s100, s100, 0x40100
	s_addc_u32 s101, s101, 0
	global_load_dwordx4 v[180:183], v201, s[100:101] nt
	s_add_u32 s100, s22, s32
	s_addc_u32 s101, s90, 0
	s_add_u32 s100, s100, 0x60100
	s_addc_u32 s101, s101, 0
	global_load_dwordx4 v[184:187], v201, s[100:101] nt
	s_add_u32 s100, s22, s32
	s_addc_u32 s101, s90, 0
	s_add_u32 s100, s100, 0x80100
	s_addc_u32 s101, s101, 0
	global_load_dwordx4 v[188:191], v201, s[100:101] nt
	v_exp_f32_e32 v106, v106
	v_exp_f32_e32 v107, v107
	v_exp_f32_e32 v108, v108
	v_exp_f32_e32 v109, v109
	v_pk_add_f32 v[106:107], v[106:107], 1.0 op_sel_hi:[1,0]
	v_pk_add_f32 v[108:109], v[108:109], 1.0 op_sel_hi:[1,0]
	v_rcp_f32_e32 v106, v106
	v_rcp_f32_e32 v107, v107
	v_rcp_f32_e32 v108, v108
	v_rcp_f32_e32 v109, v109
	v_pk_mul_f32 v[248:249], v[106:107], v[90:91]
	v_pk_fma_f32 v[248:249], v[108:109], v[92:93], v[248:249]
	v_exp_f32_e32 v114, v114
	v_exp_f32_e32 v115, v115
	v_exp_f32_e32 v116, v116
	v_exp_f32_e32 v117, v117
	v_pk_add_f32 v[114:115], v[114:115], 1.0 op_sel_hi:[1,0]
	v_pk_add_f32 v[116:117], v[116:117], 1.0 op_sel_hi:[1,0]
	v_rcp_f32_e32 v114, v114
	v_rcp_f32_e32 v115, v115
	v_rcp_f32_e32 v116, v116
	v_rcp_f32_e32 v117, v117
	v_pk_fma_f32 v[248:249], v[114:115], v[102:103], v[248:249]
	v_pk_fma_f32 v[248:249], v[116:117], v[104:105], v[248:249]
	v_exp_f32_e32 v134, v134
	v_exp_f32_e32 v135, v135
	v_exp_f32_e32 v136, v136
	v_exp_f32_e32 v137, v137
	v_pk_add_f32 v[134:135], v[134:135], 1.0 op_sel_hi:[1,0]
	v_pk_add_f32 v[136:137], v[136:137], 1.0 op_sel_hi:[1,0]
	v_rcp_f32_e32 v134, v134
	v_rcp_f32_e32 v135, v135
	v_rcp_f32_e32 v136, v136
	v_rcp_f32_e32 v137, v137
	v_pk_fma_f32 v[248:249], v[134:135], v[86:87], v[248:249]
	v_pk_fma_f32 v[248:249], v[136:137], v[88:89], v[248:249]
	v_exp_f32_e32 v138, v138
	v_exp_f32_e32 v139, v139
	v_exp_f32_e32 v140, v140
	v_exp_f32_e32 v141, v141
	v_pk_add_f32 v[138:139], v[138:139], 1.0 op_sel_hi:[1,0]
	v_pk_add_f32 v[140:141], v[140:141], 1.0 op_sel_hi:[1,0]
	v_rcp_f32_e32 v138, v138
	v_rcp_f32_e32 v139, v139
	v_rcp_f32_e32 v140, v140
	v_rcp_f32_e32 v141, v141
	v_pk_fma_f32 v[248:249], v[138:139], v[98:99], v[248:249]
	v_pk_fma_f32 v[248:249], v[140:141], v[100:101], v[248:249]
	v_exp_f32_e32 v146, v146
	v_exp_f32_e32 v147, v147
	v_exp_f32_e32 v148, v148
	v_exp_f32_e32 v149, v149
	v_pk_add_f32 v[146:147], v[146:147], 1.0 op_sel_hi:[1,0]
	v_pk_add_f32 v[148:149], v[148:149], 1.0 op_sel_hi:[1,0]
	v_rcp_f32_e32 v146, v146
	v_rcp_f32_e32 v147, v147
	v_rcp_f32_e32 v148, v148
	v_rcp_f32_e32 v149, v149
	v_pk_fma_f32 v[248:249], v[146:147], v[118:119], v[248:249]
	v_pk_fma_f32 v[248:249], v[148:149], v[120:121], v[248:249]
	v_exp_f32_e32 v150, v150
	v_exp_f32_e32 v151, v151
	v_exp_f32_e32 v152, v152
	v_exp_f32_e32 v153, v153
	v_pk_add_f32 v[150:151], v[150:151], 1.0 op_sel_hi:[1,0]
	v_pk_add_f32 v[152:153], v[152:153], 1.0 op_sel_hi:[1,0]
	v_rcp_f32_e32 v150, v150
	v_rcp_f32_e32 v151, v151
	v_rcp_f32_e32 v152, v152
	v_rcp_f32_e32 v153, v153
	v_pk_fma_f32 v[248:249], v[150:151], v[110:111], v[248:249]
	v_pk_fma_f32 v[248:249], v[152:153], v[112:113], v[248:249]
	v_exp_f32_e32 v162, v162
	v_exp_f32_e32 v163, v163
	v_exp_f32_e32 v164, v164
	v_exp_f32_e32 v165, v165
	v_pk_add_f32 v[162:163], v[162:163], 1.0 op_sel_hi:[1,0]
	v_pk_add_f32 v[164:165], v[164:165], 1.0 op_sel_hi:[1,0]
	v_rcp_f32_e32 v162, v162
	v_rcp_f32_e32 v163, v163
	v_rcp_f32_e32 v164, v164
	v_rcp_f32_e32 v165, v165
	v_pk_fma_f32 v[248:249], v[162:163], v[126:127], v[248:249]
	v_pk_fma_f32 v[248:249], v[164:165], v[128:129], v[248:249]
	v_exp_f32_e32 v174, v174
	v_exp_f32_e32 v175, v175
	v_exp_f32_e32 v176, v176
	v_exp_f32_e32 v177, v177
	v_pk_add_f32 v[174:175], v[174:175], 1.0 op_sel_hi:[1,0]
	v_pk_add_f32 v[176:177], v[176:177], 1.0 op_sel_hi:[1,0]
	v_rcp_f32_e32 v174, v174
	v_rcp_f32_e32 v175, v175
	v_rcp_f32_e32 v176, v176
	v_rcp_f32_e32 v177, v177
	v_pk_fma_f32 v[248:249], v[174:175], v[122:123], v[248:249]
	v_pk_fma_f32 v[248:249], v[176:177], v[124:125], v[248:249]
	v_add_f32_e32 v114, v248, v249
	v_mov_b32_e32 v106, v114
	s_waitcnt vmcnt(14)
	v_cmp_eq_u32_e64 s[0:1], 0, v210
	s_waitcnt lgkmcnt(0)
	s_nop 1
	v_permlane16_swap_b32_e32 v106, v114
	v_add_f32_e32 v106, v114, v106
	v_mov_b32_e32 v107, v106
	s_waitcnt lgkmcnt(0)
	s_nop 1
	v_permlane32_swap_b32_e32 v107, v106
	v_add_f32_e32 v106, v106, v107
	v_add_f32_e32 v106, v212, v106
	v_mul_f32_e32 v106, 0x3fb8aa3b, v106
	v_exp_f32_e32 v106, v106
	s_nop 0
	v_cndmask_b32_e64 v106, 0, v106, s[0:1]
	s_and_saveexec_b64 s[0:1], vcc
	s_cbranch_execz .LBB1_18
	global_store_dword v[198:199], v106, off offset:128
.LBB1_18:
	s_or_b64 exec, exec, s[0:1]
	s_add_u32 s100, s22, s32
	s_addc_u32 s101, s90, 0
	s_add_u32 s100, s100, 0xa0100
	s_addc_u32 s101, s101, 0
	global_load_dwordx4 v[136:139], v201, s[100:101] nt
	s_add_u32 s100, s22, s32
	s_addc_u32 s101, s90, 0
	s_add_u32 s100, s100, 0xc0100
	s_addc_u32 s101, s101, 0
	global_load_dwordx4 v[148:151], v201, s[100:101] nt
	s_add_u32 s100, s22, s32
	s_addc_u32 s101, s90, 0
	s_add_u32 s100, s100, 0xe0100
	s_addc_u32 s101, s101, 0
	global_load_dwordx4 v[160:163], v201, s[100:101] nt
	v_exp_f32_e32 v66, v66
	v_exp_f32_e32 v67, v67
	v_exp_f32_e32 v68, v68
	v_exp_f32_e32 v69, v69
	v_pk_add_f32 v[66:67], v[66:67], 1.0 op_sel_hi:[1,0]
	v_pk_add_f32 v[68:69], v[68:69], 1.0 op_sel_hi:[1,0]
	v_rcp_f32_e32 v66, v66
	v_rcp_f32_e32 v67, v67
	v_rcp_f32_e32 v68, v68
	v_rcp_f32_e32 v69, v69
	v_pk_mul_f32 v[248:249], v[66:67], v[102:103]
	v_pk_fma_f32 v[248:249], v[68:69], v[104:105], v[248:249]
	v_exp_f32_e32 v70, v70
	v_exp_f32_e32 v71, v71
	v_exp_f32_e32 v72, v72
	v_exp_f32_e32 v73, v73
	v_pk_add_f32 v[70:71], v[70:71], 1.0 op_sel_hi:[1,0]
	v_pk_add_f32 v[72:73], v[72:73], 1.0 op_sel_hi:[1,0]
	v_rcp_f32_e32 v70, v70
	v_rcp_f32_e32 v71, v71
	v_rcp_f32_e32 v72, v72
	v_rcp_f32_e32 v73, v73
	v_pk_fma_f32 v[248:249], v[70:71], v[90:91], v[248:249]
	v_pk_fma_f32 v[248:249], v[72:73], v[92:93], v[248:249]
	v_exp_f32_e32 v74, v74
	v_exp_f32_e32 v75, v75
	v_exp_f32_e32 v76, v76
	v_exp_f32_e32 v77, v77
	v_pk_add_f32 v[74:75], v[74:75], 1.0 op_sel_hi:[1,0]
	v_pk_add_f32 v[76:77], v[76:77], 1.0 op_sel_hi:[1,0]
	v_rcp_f32_e32 v74, v74
	v_rcp_f32_e32 v75, v75
	v_rcp_f32_e32 v76, v76
	v_rcp_f32_e32 v77, v77
	v_pk_fma_f32 v[248:249], v[74:75], v[98:99], v[248:249]
	v_pk_fma_f32 v[248:249], v[76:77], v[100:101], v[248:249]
	v_exp_f32_e32 v78, v78
	v_exp_f32_e32 v79, v79
	v_exp_f32_e32 v80, v80
	v_exp_f32_e32 v81, v81
	v_pk_add_f32 v[78:79], v[78:79], 1.0 op_sel_hi:[1,0]
	v_pk_add_f32 v[80:81], v[80:81], 1.0 op_sel_hi:[1,0]
	v_rcp_f32_e32 v78, v78
	v_rcp_f32_e32 v79, v79
	v_rcp_f32_e32 v80, v80
	v_rcp_f32_e32 v81, v81
	v_pk_fma_f32 v[248:249], v[78:79], v[86:87], v[248:249]
	v_pk_fma_f32 v[248:249], v[80:81], v[88:89], v[248:249]
	v_exp_f32_e32 v82, v82
	v_exp_f32_e32 v83, v83
	v_exp_f32_e32 v84, v84
	v_exp_f32_e32 v85, v85
	v_pk_add_f32 v[82:83], v[82:83], 1.0 op_sel_hi:[1,0]
	v_pk_add_f32 v[84:85], v[84:85], 1.0 op_sel_hi:[1,0]
	v_rcp_f32_e32 v82, v82
	v_rcp_f32_e32 v83, v83
	v_rcp_f32_e32 v84, v84
	v_rcp_f32_e32 v85, v85
	v_pk_fma_f32 v[248:249], v[82:83], v[118:119], v[248:249]
	v_pk_fma_f32 v[248:249], v[84:85], v[120:121], v[248:249]
	v_exp_f32_e32 v94, v94
	v_exp_f32_e32 v95, v95
	v_exp_f32_e32 v96, v96
	v_exp_f32_e32 v97, v97
	v_pk_add_f32 v[94:95], v[94:95], 1.0 op_sel_hi:[1,0]
	v_pk_add_f32 v[96:97], v[96:97], 1.0 op_sel_hi:[1,0]
	v_rcp_f32_e32 v94, v94
	v_rcp_f32_e32 v95, v95
	v_rcp_f32_e32 v96, v96
	v_rcp_f32_e32 v97, v97
	v_pk_fma_f32 v[248:249], v[94:95], v[110:111], v[248:249]
	v_pk_fma_f32 v[248:249], v[96:97], v[112:113], v[248:249]
	v_exp_f32_e32 v130, v130
	v_exp_f32_e32 v131, v131
	v_exp_f32_e32 v132, v132
	v_exp_f32_e32 v133, v133
	v_pk_add_f32 v[130:131], v[130:131], 1.0 op_sel_hi:[1,0]
	v_pk_add_f32 v[132:133], v[132:133], 1.0 op_sel_hi:[1,0]
	v_rcp_f32_e32 v130, v130
	v_rcp_f32_e32 v131, v131
	v_rcp_f32_e32 v132, v132
	v_rcp_f32_e32 v133, v133
	v_pk_fma_f32 v[248:249], v[130:131], v[126:127], v[248:249]
	v_pk_fma_f32 v[248:249], v[132:133], v[128:129], v[248:249]
	v_exp_f32_e32 v142, v142
	v_exp_f32_e32 v143, v143
	v_exp_f32_e32 v144, v144
	v_exp_f32_e32 v145, v145
	v_pk_add_f32 v[142:143], v[142:143], 1.0 op_sel_hi:[1,0]
	v_pk_add_f32 v[144:145], v[144:145], 1.0 op_sel_hi:[1,0]
	v_rcp_f32_e32 v142, v142
	v_rcp_f32_e32 v143, v143
	v_rcp_f32_e32 v144, v144
	v_rcp_f32_e32 v145, v145
	v_pk_fma_f32 v[248:249], v[142:143], v[122:123], v[248:249]
	v_pk_fma_f32 v[248:249], v[144:145], v[124:125], v[248:249]
	v_add_f32_e32 v66, v248, v249
	v_mov_b32_e32 v67, v66
	s_waitcnt vmcnt(16)
	v_cmp_eq_u32_e64 s[0:1], 0, v209
	s_waitcnt lgkmcnt(0)
	s_nop 1
	v_permlane16_swap_b32_e32 v67, v66
	v_add_f32_e32 v66, v66, v67
	v_mov_b32_e32 v67, v66
	s_waitcnt lgkmcnt(0)
	s_nop 1
	v_permlane32_swap_b32_e32 v67, v66
	v_add_f32_e32 v66, v66, v67
	v_add_f32_e32 v66, v212, v66
	v_mul_f32_e32 v66, 0x3fb8aa3b, v66
	v_exp_f32_e32 v66, v66
	s_nop 0
	v_cndmask_b32_e64 v66, 0, v66, s[0:1]
	s_and_saveexec_b64 s[0:1], vcc
	s_cbranch_execz .LBB1_20
	global_store_dword v[198:199], v66, off offset:192
